# k_bfinal x->fp16 blocks: all 14 float4 loads in flight before converting/storing (was 14 serialized load-wait round trips)
# speedup vs baseline: 1.0057x; 1.0057x over previous
.LBB1_69:
	s_and_b64 vcc, exec, s[4:5]
	s_cbranch_vccz .LBB1_112
	s_load_dwordx4 s[4:7], s[0:1], 0x30
	s_lshl_b32 s2, s2, 10
	s_add_i32 s2, s2, 0xfffd8c00
	v_or_b32_e32 v0, s2, v0
	v_lshlrev_b32_e32 v1, 4, v0
	v_lshlrev_b32_e32 v2, 3, v0
	v_cmp_gt_u32_e32 vcc, 0x800, v0
	s_waitcnt lgkmcnt(0)
	global_load_dwordx4 v[4:7], v1, s[4:5]
	s_add_u32 s4, s4, 0x180000
	s_addc_u32 s5, s5, 0
	global_load_dwordx4 v[8:11], v1, s[4:5]
	s_add_u32 s4, s4, 0x180000
	s_addc_u32 s5, s5, 0
	global_load_dwordx4 v[12:15], v1, s[4:5]
	s_add_u32 s4, s4, 0x180000
	s_addc_u32 s5, s5, 0
	global_load_dwordx4 v[16:19], v1, s[4:5]
	s_add_u32 s4, s4, 0x180000
	s_addc_u32 s5, s5, 0
	global_load_dwordx4 v[20:23], v1, s[4:5]
	s_add_u32 s4, s4, 0x180000
	s_addc_u32 s5, s5, 0
	global_load_dwordx4 v[24:27], v1, s[4:5]
	s_add_u32 s4, s4, 0x180000
	s_addc_u32 s5, s5, 0
	global_load_dwordx4 v[28:31], v1, s[4:5]
	s_add_u32 s4, s4, 0x180000
	s_addc_u32 s5, s5, 0
	global_load_dwordx4 v[32:35], v1, s[4:5]
	s_add_u32 s4, s4, 0x180000
	s_addc_u32 s5, s5, 0
	global_load_dwordx4 v[36:39], v1, s[4:5]
	s_add_u32 s4, s4, 0x180000
	s_addc_u32 s5, s5, 0
	global_load_dwordx4 v[40:43], v1, s[4:5]
	s_add_u32 s4, s4, 0x180000
	s_addc_u32 s5, s5, 0
	global_load_dwordx4 v[44:47], v1, s[4:5]
	s_add_u32 s4, s4, 0x180000
	s_addc_u32 s5, s5, 0
	global_load_dwordx4 v[48:51], v1, s[4:5]
	s_add_u32 s4, s4, 0x180000
	s_addc_u32 s5, s5, 0
	global_load_dwordx4 v[52:55], v1, s[4:5]
	s_add_u32 s4, s4, 0x180000
	s_addc_u32 s5, s5, 0
	s_and_saveexec_b64 s[8:9], vcc
	global_load_dwordx4 v[56:59], v1, s[4:5]
	s_mov_b64 exec, s[8:9]
	s_waitcnt vmcnt(12)
	v_cvt_pk_f16_f32 v60, v4, v5
	v_cvt_pk_f16_f32 v61, v6, v7
	global_store_dwordx2 v2, v[60:61], s[6:7]
	s_add_u32 s6, s6, 0xc0000
	s_addc_u32 s7, s7, 0
	s_waitcnt vmcnt(12)
	v_cvt_pk_f16_f32 v62, v8, v9
	v_cvt_pk_f16_f32 v63, v10, v11
	global_store_dwordx2 v2, v[62:63], s[6:7]
	s_add_u32 s6, s6, 0xc0000
	s_addc_u32 s7, s7, 0
	s_waitcnt vmcnt(12)
	v_cvt_pk_f16_f32 v60, v12, v13
	v_cvt_pk_f16_f32 v61, v14, v15
	global_store_dwordx2 v2, v[60:61], s[6:7]
	s_add_u32 s6, s6, 0xc0000
	s_addc_u32 s7, s7, 0
	s_waitcnt vmcnt(12)
	v_cvt_pk_f16_f32 v62, v16, v17
	v_cvt_pk_f16_f32 v63, v18, v19
	global_store_dwordx2 v2, v[62:63], s[6:7]
	s_add_u32 s6, s6, 0xc0000
	s_addc_u32 s7, s7, 0
	s_waitcnt vmcnt(12)
	v_cvt_pk_f16_f32 v60, v20, v21
	v_cvt_pk_f16_f32 v61, v22, v23
	global_store_dwordx2 v2, v[60:61], s[6:7]
	s_add_u32 s6, s6, 0xc0000
	s_addc_u32 s7, s7, 0
	s_waitcnt vmcnt(12)
	v_cvt_pk_f16_f32 v62, v24, v25
	v_cvt_pk_f16_f32 v63, v26, v27
	global_store_dwordx2 v2, v[62:63], s[6:7]
	s_add_u32 s6, s6, 0xc0000
	s_addc_u32 s7, s7, 0
	s_waitcnt vmcnt(12)
	v_cvt_pk_f16_f32 v60, v28, v29
	v_cvt_pk_f16_f32 v61, v30, v31
	global_store_dwordx2 v2, v[60:61], s[6:7]
	s_add_u32 s6, s6, 0xc0000
	s_addc_u32 s7, s7, 0
	s_waitcnt vmcnt(12)
	v_cvt_pk_f16_f32 v62, v32, v33
	v_cvt_pk_f16_f32 v63, v34, v35
	global_store_dwordx2 v2, v[62:63], s[6:7]
	s_add_u32 s6, s6, 0xc0000
	s_addc_u32 s7, s7, 0
	s_waitcnt vmcnt(12)
	v_cvt_pk_f16_f32 v60, v36, v37
	v_cvt_pk_f16_f32 v61, v38, v39
	global_store_dwordx2 v2, v[60:61], s[6:7]
	s_add_u32 s6, s6, 0xc0000
	s_addc_u32 s7, s7, 0
	s_waitcnt vmcnt(12)
	v_cvt_pk_f16_f32 v62, v40, v41
	v_cvt_pk_f16_f32 v63, v42, v43
	global_store_dwordx2 v2, v[62:63], s[6:7]
	s_add_u32 s6, s6, 0xc0000
	s_addc_u32 s7, s7, 0
	s_waitcnt vmcnt(12)
	v_cvt_pk_f16_f32 v60, v44, v45
	v_cvt_pk_f16_f32 v61, v46, v47
	global_store_dwordx2 v2, v[60:61], s[6:7]
	s_add_u32 s6, s6, 0xc0000
	s_addc_u32 s7, s7, 0
	s_waitcnt vmcnt(12)
	v_cvt_pk_f16_f32 v62, v48, v49
	v_cvt_pk_f16_f32 v63, v50, v51
	global_store_dwordx2 v2, v[62:63], s[6:7]
	s_add_u32 s6, s6, 0xc0000
	s_addc_u32 s7, s7, 0
	s_waitcnt vmcnt(12)
	v_cvt_pk_f16_f32 v60, v52, v53
	v_cvt_pk_f16_f32 v61, v54, v55
	global_store_dwordx2 v2, v[60:61], s[6:7]
	s_add_u32 s6, s6, 0xc0000
	s_addc_u32 s7, s7, 0
	s_and_saveexec_b64 s[8:9], vcc
	s_waitcnt vmcnt(0)
	v_cvt_pk_f16_f32 v62, v56, v57
	v_cvt_pk_f16_f32 v63, v58, v59
	global_store_dwordx2 v2, v[62:63], s[6:7]
.LBB1_112:
	s_endpgm
.LBB1_127:
	s_mov_b32 s6, 0xfffc
	v_and_b32_sdwa v1, v18, s6 dst_sel:DWORD dst_unused:UNUSED_PAD src0_sel:WORD_1 src1_sel:DWORD
	ds_read_b32 v1, v1 offset:8192
	s_movk_i32 s6, 0x3040
	v_lshlrev_b32_e32 v3, 3, v29
	v_and_b32_e32 v18, 0x3ffff, v18
	s_waitcnt lgkmcnt(0)
	v_lshlrev_b32_e32 v1, 3, v1
	v_add3_u32 v1, s6, v1, v3
	ds_write_b64 v1, v[18:19]
	s_or_b64 exec, exec, s[4:5]
	v_cmp_lt_i32_e32 vcc, -1, v4
	s_and_saveexec_b64 s[4:5], vcc
	s_cbranch_execz .LBB1_57
